# grid barrier: L1 invalidate issued at arrival instead of after release
# speedup vs baseline: 1.0101x; 1.0101x over previous
; __device__ __forceinline__ unsigned xb_ld(unsigned* p)              { return __hip_atomic_load(p, __ATOMIC_RELAXED, __HIP_MEMORY_SCOPE_AGENT); }
; __device__ __forceinline__ unsigned xb_add(unsigned* p, unsigned v) { return __hip_atomic_fetch_add(p, v, __ATOMIC_RELAXED, __HIP_MEMORY_SCOPE_AGENT); }
; #define XB_SPIN(cond, bar) do { unsigned _sp = 0; while (cond) { __builtin_amdgcn_s_sleep(1); \
;     if ((++_sp & 255u) == 0u) { if (xb_ld(&(bar)[XB_TMO])) break; if (_sp > XB_SPIN_CAP) { atomicAdd(&(bar)[XB_TMO], 1u); break; } } } } while (0)
; __device__ __forceinline__ void xcd_barrier(const XcdBarrier& b) {
;     ...
;         unsigned nloc = b.st[0], nx = b.st[1];
;         if (nloc == 0u) { xcd_barrier_complete(bar, b.x, nloc, nx); b.st[0] = nloc; b.st[1] = nx; }
;         const unsigned old = xb_add(&bar[XB_XSUB(b.x)], 1u);
;         const unsigned gen = old / nloc;
;         if (old + 1u == (gen + 1u) * nloc) {
;             __builtin_amdgcn_fence(__ATOMIC_RELEASE, "agent");
;             asm volatile("s_waitcnt vmcnt(0)" ::: "memory");
;             const unsigned og = xb_add(&bar[XB_TOP], 1u);
;             const unsigned tg = og / nx;
;             if (og + 1u == (tg + 1u) * nx) xb_add(&bar[XB_TOPGEN], 1u);
;             else XB_SPIN(xb_ld(&bar[XB_TOPGEN]) == tg, bar);
.LBB0_254:
	s_lshl_b32 s3, s3, 6
	s_add_i32 s6, s3, 0x500
	s_mov_b32 s7, 0
	s_lshl_b64 s[4:5], s[6:7], 2
	s_add_u32 s4, s38, s4
	s_addc_u32 s5, s39, s5
	v_mov_b32_e32 v1, 1
	v_mov_b64_e32 v[6:7], s[4:5]
	flat_atomic_add v1, v[6:7], v1 sc0
	buffer_inv sc1
	v_cvt_f32_u32_e32 v3, v4
	v_sub_u32_e32 v5, 0, v4
	v_rcp_iflag_f32_e32 v3, v3
	s_nop 0
	v_mul_f32_e32 v3, 0x4f7ffffe, v3
	v_cvt_u32_f32_e32 v3, v3
	v_mul_lo_u32 v5, v5, v3
	v_mul_hi_u32 v5, v3, v5
	v_add_u32_e32 v3, v3, v5
	s_waitcnt vmcnt(0) lgkmcnt(0)
	v_mul_hi_u32 v3, v1, v3
	v_mul_lo_u32 v5, v3, v4
	v_add_u32_e32 v6, 1, v1
	v_sub_u32_e32 v1, v1, v5
	v_add_u32_e32 v7, 1, v3
	v_cmp_ge_u32_e32 vcc, v1, v4
	v_sub_u32_e32 v5, v1, v4
	s_nop 0
	v_cndmask_b32_e32 v3, v3, v7, vcc
	v_cndmask_b32_e32 v1, v1, v5, vcc
	v_add_u32_e32 v5, 1, v3
	v_cmp_ge_u32_e32 vcc, v1, v4
	s_nop 1
	v_cndmask_b32_e32 v1, v3, v5, vcc
	v_mad_u64_u32 v[4:5], s[4:5], v4, v1, v[4:5]
	v_cmp_ne_u32_e32 vcc, v6, v4
	s_and_saveexec_b64 s[4:5], vcc
	s_xor_b64 s[4:5], exec, s[4:5]
	s_cbranch_execz .LBB0_267
	s_add_i32 s6, s3, 0x900
	s_lshl_b64 s[6:7], s[6:7], 2
	s_add_u32 s8, s38, s6
	s_addc_u32 s9, s39, s7
	v_mov_b64_e32 v[2:3], s[8:9]
	flat_load_dword v2, v[2:3] sc1
	s_waitcnt vmcnt(0) lgkmcnt(0)
	v_cmp_eq_u32_e32 vcc, v2, v1
	s_and_saveexec_b64 s[6:7], vcc
	s_cbranch_execz .LBB0_266
	s_mov_b32 s26, 1
	s_mov_b64 s[10:11], 0
	s_branch .LBB0_258

; __device__ __forceinline__ unsigned xb_ld(unsigned* p)              { return __hip_atomic_load(p, __ATOMIC_RELAXED, __HIP_MEMORY_SCOPE_AGENT); }
; #define XB_SPIN(cond, bar) do { unsigned _sp = 0; while (cond) { __builtin_amdgcn_s_sleep(1); \
;     if ((++_sp & 255u) == 0u) { if (xb_ld(&(bar)[XB_TMO])) break; if (_sp > XB_SPIN_CAP) { atomicAdd(&(bar)[XB_TMO], 1u); break; } } } } while (0)
; __device__ __forceinline__ void xcd_barrier(const XcdBarrier& b) {
;     ...
;             XB_SPIN(xb_ld(&bar[XB_XGEN(b.x)]) == gen, bar);
;             __builtin_amdgcn_fence(__ATOMIC_ACQUIRE, "agent");
;             asm volatile("s_waitcnt vmcnt(0)" ::: "memory");
.LBB0_266:
	s_or_b64 exec, exec, s[6:7]
	s_waitcnt vmcnt(0) lgkmcnt(0)
	s_waitcnt vmcnt(0)

; __device__ __forceinline__ unsigned xb_add(unsigned* p, unsigned v) { return __hip_atomic_fetch_add(p, v, __ATOMIC_RELAXED, __HIP_MEMORY_SCOPE_AGENT); }
; __device__ __forceinline__ void xcd_barrier(const XcdBarrier& b) {
;     ...
;             __builtin_amdgcn_fence(__ATOMIC_ACQUIRE, "agent");
;             xb_add(&bar[XB_XGEN(b.x)], 1u);
;             asm volatile("s_waitcnt vmcnt(0)" ::: "memory");
.LBB0_282:
	s_or_b64 exec, exec, s[4:5]
	s_add_i32 s4, s3, 0x900
	s_mov_b32 s5, 0
	s_lshl_b64 s[4:5], s[4:5], 2
	s_add_u32 s4, s38, s4
	s_addc_u32 s5, s39, s5
	v_mov_b32_e32 v1, 1
	v_mov_b64_e32 v[2:3], s[4:5]
	s_waitcnt vmcnt(0) lgkmcnt(0)
	flat_atomic_add v[2:3], v1
	s_waitcnt vmcnt(0)

; __device__ __forceinline__ unsigned xb_add(unsigned* p, unsigned v) { return __hip_atomic_fetch_add(p, v, __ATOMIC_RELAXED, __HIP_MEMORY_SCOPE_AGENT); }
; __device__ __forceinline__ void xcd_barrier(const XcdBarrier& b) {
;     ...
;             __builtin_amdgcn_fence(__ATOMIC_ACQUIRE, "agent");
;             xb_add(&bar[XB_XGEN(b.x)], 1u);
;             asm volatile("s_waitcnt vmcnt(0)" ::: "memory");
.LBB0_284:
	s_or_b64 exec, exec, s[8:9]
	s_add_i32 s88, s2, 0x900
	s_lshl_b64 s[2:3], s[88:89], 2
	s_add_u32 s2, s44, s2
	s_addc_u32 s3, s45, s3
	v_mov_b64_e32 v[2:3], s[2:3]
	s_waitcnt vmcnt(0) lgkmcnt(0)
	flat_atomic_add v[2:3], v235
	s_waitcnt vmcnt(0)

; __device__ __forceinline__ unsigned xb_ld(unsigned* p)              { return __hip_atomic_load(p, __ATOMIC_RELAXED, __HIP_MEMORY_SCOPE_AGENT); }
; __device__ __forceinline__ unsigned xb_add(unsigned* p, unsigned v) { return __hip_atomic_fetch_add(p, v, __ATOMIC_RELAXED, __HIP_MEMORY_SCOPE_AGENT); }
; #define XB_SPIN(cond, bar) do { unsigned _sp = 0; while (cond) { __builtin_amdgcn_s_sleep(1); \
;     if ((++_sp & 255u) == 0u) { if (xb_ld(&(bar)[XB_TMO])) break; if (_sp > XB_SPIN_CAP) { atomicAdd(&(bar)[XB_TMO], 1u); break; } } } } while (0)
; __device__ __forceinline__ void xcd_barrier(const XcdBarrier& b) {
;     ...
;         unsigned nloc = b.st[0], nx = b.st[1];
;         if (nloc == 0u) { xcd_barrier_complete(bar, b.x, nloc, nx); b.st[0] = nloc; b.st[1] = nx; }
;         const unsigned old = xb_add(&bar[XB_XSUB(b.x)], 1u);
;         const unsigned gen = old / nloc;
;         if (old + 1u == (gen + 1u) * nloc) {
;             __builtin_amdgcn_fence(__ATOMIC_RELEASE, "agent");
;             asm volatile("s_waitcnt vmcnt(0)" ::: "memory");
;             const unsigned og = xb_add(&bar[XB_TOP], 1u);
;             const unsigned tg = og / nx;
;             if (og + 1u == (tg + 1u) * nx) xb_add(&bar[XB_TOPGEN], 1u);
;             else XB_SPIN(xb_ld(&bar[XB_TOPGEN]) == tg, bar);
.LBB0_612:
	s_lshl_b32 s2, s2, 6
	s_add_i32 s88, s2, 0x500
	s_lshl_b64 s[6:7], s[88:89], 2
	s_add_u32 s6, s44, s6
	s_addc_u32 s7, s45, s7
	v_mov_b64_e32 v[4:5], s[6:7]
	flat_atomic_add v3, v[4:5], v235 sc0
	buffer_inv sc1
	v_cvt_f32_u32_e32 v4, v2
	v_sub_u32_e32 v5, 0, v2
	v_rcp_iflag_f32_e32 v4, v4
	s_nop 0
	v_mul_f32_e32 v4, 0x4f7ffffe, v4
	v_cvt_u32_f32_e32 v4, v4
	v_mul_lo_u32 v5, v5, v4
	v_mul_hi_u32 v5, v4, v5
	v_add_u32_e32 v4, v4, v5
	s_waitcnt vmcnt(0) lgkmcnt(0)
	v_mul_hi_u32 v4, v3, v4
	v_mul_lo_u32 v5, v4, v2
	v_add_u32_e32 v6, 1, v3
	v_sub_u32_e32 v3, v3, v5
	v_add_u32_e32 v7, 1, v4
	v_sub_u32_e32 v5, v3, v2
	v_cmp_ge_u32_e32 vcc, v3, v2
	s_nop 1
	v_cndmask_b32_e32 v4, v4, v7, vcc
	v_cndmask_b32_e32 v3, v3, v5, vcc
	v_add_u32_e32 v5, 1, v4
	v_cmp_ge_u32_e32 vcc, v3, v2
	s_nop 1
	v_cndmask_b32_e32 v3, v4, v5, vcc
	v_mad_u64_u32 v[4:5], s[6:7], v2, v3, v[2:3]
	v_cmp_ne_u32_e32 vcc, v6, v4
	s_and_saveexec_b64 s[6:7], vcc
	s_xor_b64 s[8:9], exec, s[6:7]
	s_cbranch_execz .LBB0_625
	s_add_i32 s88, s2, 0x900
	s_lshl_b64 s[6:7], s[88:89], 2
	s_add_u32 s12, s44, s6
	s_addc_u32 s13, s45, s7
	v_mov_b64_e32 v[4:5], s[12:13]
	flat_load_dword v0, v[4:5] sc1
	s_waitcnt vmcnt(0) lgkmcnt(0)
	v_cmp_eq_u32_e32 vcc, v0, v3
	s_and_saveexec_b64 s[10:11], vcc
	s_cbranch_execz .LBB0_624
	s_mov_b32 s3, 1
	s_mov_b64 s[14:15], 0
	s_branch .LBB0_616

; __device__ __forceinline__ unsigned xb_ld(unsigned* p)              { return __hip_atomic_load(p, __ATOMIC_RELAXED, __HIP_MEMORY_SCOPE_AGENT); }
; #define XB_SPIN(cond, bar) do { unsigned _sp = 0; while (cond) { __builtin_amdgcn_s_sleep(1); \
;     if ((++_sp & 255u) == 0u) { if (xb_ld(&(bar)[XB_TMO])) break; if (_sp > XB_SPIN_CAP) { atomicAdd(&(bar)[XB_TMO], 1u); break; } } } } while (0)
; __device__ __forceinline__ void xcd_barrier(const XcdBarrier& b) {
;     ...
;             XB_SPIN(xb_ld(&bar[XB_XGEN(b.x)]) == gen, bar);
;             __builtin_amdgcn_fence(__ATOMIC_ACQUIRE, "agent");
;             asm volatile("s_waitcnt vmcnt(0)" ::: "memory");
.LBB0_624:
	s_or_b64 exec, exec, s[10:11]
	s_waitcnt vmcnt(0) lgkmcnt(0)
	s_waitcnt vmcnt(0)

; __device__ __forceinline__ unsigned xb_ld(unsigned* p)              { return __hip_atomic_load(p, __ATOMIC_RELAXED, __HIP_MEMORY_SCOPE_AGENT); }
; __device__ __forceinline__ unsigned xb_add(unsigned* p, unsigned v) { return __hip_atomic_fetch_add(p, v, __ATOMIC_RELAXED, __HIP_MEMORY_SCOPE_AGENT); }
; #define XB_SPIN(cond, bar) do { unsigned _sp = 0; while (cond) { __builtin_amdgcn_s_sleep(1); \
;     if ((++_sp & 255u) == 0u) { if (xb_ld(&(bar)[XB_TMO])) break; if (_sp > XB_SPIN_CAP) { atomicAdd(&(bar)[XB_TMO], 1u); break; } } } } while (0)
; __device__ __forceinline__ void xcd_barrier(const XcdBarrier& b) {
;     ...
;         unsigned nloc = b.st[0], nx = b.st[1];
;         if (nloc == 0u) { xcd_barrier_complete(bar, b.x, nloc, nx); b.st[0] = nloc; b.st[1] = nx; }
;         const unsigned old = xb_add(&bar[XB_XSUB(b.x)], 1u);
;         const unsigned gen = old / nloc;
;         if (old + 1u == (gen + 1u) * nloc) {
;             __builtin_amdgcn_fence(__ATOMIC_RELEASE, "agent");
;             asm volatile("s_waitcnt vmcnt(0)" ::: "memory");
;             const unsigned og = xb_add(&bar[XB_TOP], 1u);
;             const unsigned tg = og / nx;
;             if (og + 1u == (tg + 1u) * nx) xb_add(&bar[XB_TOPGEN], 1u);
;             else XB_SPIN(xb_ld(&bar[XB_TOPGEN]) == tg, bar);
.LBB0_734:
	s_lshl_b32 s2, s2, 6
	s_add_i32 s88, s2, 0x500
	s_lshl_b64 s[6:7], s[88:89], 2
	s_add_u32 s6, s44, s6
	s_addc_u32 s7, s45, s7
	v_mov_b64_e32 v[4:5], s[6:7]
	flat_atomic_add v4, v[4:5], v235 sc0
	buffer_inv sc1
	v_cvt_f32_u32_e32 v3, v2
	v_sub_u32_e32 v5, 0, v2
	v_rcp_iflag_f32_e32 v3, v3
	s_nop 0
	v_mul_f32_e32 v3, 0x4f7ffffe, v3
	v_cvt_u32_f32_e32 v3, v3
	v_mul_lo_u32 v5, v5, v3
	v_mul_hi_u32 v5, v3, v5
	v_add_u32_e32 v3, v3, v5
	s_waitcnt vmcnt(0) lgkmcnt(0)
	v_mul_hi_u32 v3, v4, v3
	v_mul_lo_u32 v5, v3, v2
	v_sub_u32_e32 v5, v4, v5
	v_cmp_ge_u32_e32 vcc, v5, v2
	v_add_u32_e32 v6, 1, v3
	s_nop 0
	v_cndmask_b32_e32 v3, v3, v6, vcc
	v_sub_u32_e32 v6, v5, v2
	v_cndmask_b32_e32 v5, v5, v6, vcc
	v_cmp_ge_u32_e32 vcc, v5, v2
	v_add_u32_e32 v5, 1, v3
	v_add_u32_e32 v6, 1, v4
	v_cndmask_b32_e32 v3, v3, v5, vcc
	v_mad_u64_u32 v[4:5], s[6:7], v2, v3, v[2:3]
	v_cmp_ne_u32_e32 vcc, v6, v4
	s_and_saveexec_b64 s[6:7], vcc
	s_xor_b64 s[8:9], exec, s[6:7]
	s_cbranch_execz .LBB0_747
	s_add_i32 s88, s2, 0x900
	s_lshl_b64 s[6:7], s[88:89], 2
	s_add_u32 s12, s44, s6
	s_addc_u32 s13, s45, s7
	v_mov_b64_e32 v[4:5], s[12:13]
	flat_load_dword v0, v[4:5] sc1
	s_waitcnt vmcnt(0) lgkmcnt(0)
	v_cmp_eq_u32_e32 vcc, v0, v3
	s_and_saveexec_b64 s[10:11], vcc
	s_cbranch_execz .LBB0_746
	s_mov_b32 s3, 1
	s_mov_b64 s[14:15], 0
	s_branch .LBB0_738

; __device__ __forceinline__ unsigned xb_ld(unsigned* p)              { return __hip_atomic_load(p, __ATOMIC_RELAXED, __HIP_MEMORY_SCOPE_AGENT); }
; __device__ __forceinline__ unsigned xb_add(unsigned* p, unsigned v) { return __hip_atomic_fetch_add(p, v, __ATOMIC_RELAXED, __HIP_MEMORY_SCOPE_AGENT); }
; #define XB_SPIN(cond, bar) do { unsigned _sp = 0; while (cond) { __builtin_amdgcn_s_sleep(1); \
;     if ((++_sp & 255u) == 0u) { if (xb_ld(&(bar)[XB_TMO])) break; if (_sp > XB_SPIN_CAP) { atomicAdd(&(bar)[XB_TMO], 1u); break; } } } } while (0)
; __device__ __forceinline__ void xcd_barrier(const XcdBarrier& b) {
;     ...
;         unsigned nloc = b.st[0], nx = b.st[1];
;         if (nloc == 0u) { xcd_barrier_complete(bar, b.x, nloc, nx); b.st[0] = nloc; b.st[1] = nx; }
;         const unsigned old = xb_add(&bar[XB_XSUB(b.x)], 1u);
;         const unsigned gen = old / nloc;
;         if (old + 1u == (gen + 1u) * nloc) {
;             __builtin_amdgcn_fence(__ATOMIC_RELEASE, "agent");
;             asm volatile("s_waitcnt vmcnt(0)" ::: "memory");
;             const unsigned og = xb_add(&bar[XB_TOP], 1u);
;             const unsigned tg = og / nx;
;             if (og + 1u == (tg + 1u) * nx) xb_add(&bar[XB_TOPGEN], 1u);
;             else XB_SPIN(xb_ld(&bar[XB_TOPGEN]) == tg, bar);
.LBB0_991:
	s_lshl_b32 s2, s2, 6
	s_add_i32 s88, s2, 0x500
	s_lshl_b64 s[6:7], s[88:89], 2
	s_add_u32 s6, s48, s6
	s_addc_u32 s7, s49, s7
	v_mov_b64_e32 v[4:5], s[6:7]
	flat_atomic_add v4, v[4:5], v235 sc0
	buffer_inv sc1
	v_cvt_f32_u32_e32 v3, v2
	v_sub_u32_e32 v5, 0, v2
	v_rcp_iflag_f32_e32 v3, v3
	s_nop 0
	v_mul_f32_e32 v3, 0x4f7ffffe, v3
	v_cvt_u32_f32_e32 v3, v3
	v_mul_lo_u32 v5, v5, v3
	v_mul_hi_u32 v5, v3, v5
	v_add_u32_e32 v3, v3, v5
	s_waitcnt vmcnt(0) lgkmcnt(0)
	v_mul_hi_u32 v3, v4, v3
	v_mul_lo_u32 v5, v3, v2
	v_sub_u32_e32 v5, v4, v5
	v_cmp_ge_u32_e32 vcc, v5, v2
	v_add_u32_e32 v6, 1, v3
	s_nop 0
	v_cndmask_b32_e32 v3, v3, v6, vcc
	v_sub_u32_e32 v6, v5, v2
	v_cndmask_b32_e32 v5, v5, v6, vcc
	v_cmp_ge_u32_e32 vcc, v5, v2
	v_add_u32_e32 v5, 1, v3
	v_add_u32_e32 v6, 1, v4
	v_cndmask_b32_e32 v3, v3, v5, vcc
	v_mad_u64_u32 v[4:5], s[6:7], v2, v3, v[2:3]
	v_cmp_ne_u32_e32 vcc, v6, v4
	s_and_saveexec_b64 s[6:7], vcc
	s_xor_b64 s[10:11], exec, s[6:7]
	s_cbranch_execz .LBB0_1004
	s_add_i32 s88, s2, 0x900
	s_lshl_b64 s[6:7], s[88:89], 2
	s_add_u32 s14, s48, s6
	s_addc_u32 s15, s49, s7
	v_mov_b64_e32 v[4:5], s[14:15]
	flat_load_dword v0, v[4:5] sc1
	s_waitcnt vmcnt(0) lgkmcnt(0)
	v_cmp_eq_u32_e32 vcc, v0, v3
	s_and_saveexec_b64 s[12:13], vcc
	s_cbranch_execz .LBB0_1003
	s_mov_b32 s3, 1
	s_mov_b64 s[16:17], 0
	s_branch .LBB0_995

; __device__ __forceinline__ unsigned xb_ld(unsigned* p)              { return __hip_atomic_load(p, __ATOMIC_RELAXED, __HIP_MEMORY_SCOPE_AGENT); }
; #define XB_SPIN(cond, bar) do { unsigned _sp = 0; while (cond) { __builtin_amdgcn_s_sleep(1); \
;     if ((++_sp & 255u) == 0u) { if (xb_ld(&(bar)[XB_TMO])) break; if (_sp > XB_SPIN_CAP) { atomicAdd(&(bar)[XB_TMO], 1u); break; } } } } while (0)
; __device__ __forceinline__ void xcd_barrier(const XcdBarrier& b) {
;     ...
;             XB_SPIN(xb_ld(&bar[XB_XGEN(b.x)]) == gen, bar);
;             __builtin_amdgcn_fence(__ATOMIC_ACQUIRE, "agent");
;             asm volatile("s_waitcnt vmcnt(0)" ::: "memory");
.LBB0_1003:
	s_or_b64 exec, exec, s[12:13]
	s_waitcnt vmcnt(0) lgkmcnt(0)
	s_waitcnt vmcnt(0)

; __device__ __forceinline__ unsigned xb_add(unsigned* p, unsigned v) { return __hip_atomic_fetch_add(p, v, __ATOMIC_RELAXED, __HIP_MEMORY_SCOPE_AGENT); }
; __device__ __forceinline__ void xcd_barrier(const XcdBarrier& b) {
;     ...
;             __builtin_amdgcn_fence(__ATOMIC_ACQUIRE, "agent");
;             xb_add(&bar[XB_XGEN(b.x)], 1u);
;             asm volatile("s_waitcnt vmcnt(0)" ::: "memory");
.LBB0_1019:
	s_or_b64 exec, exec, s[10:11]
	s_add_i32 s88, s2, 0x900
	s_lshl_b64 s[2:3], s[88:89], 2
	s_add_u32 s2, s48, s2
	s_addc_u32 s3, s49, s3
	v_mov_b64_e32 v[2:3], s[2:3]
	s_waitcnt vmcnt(0) lgkmcnt(0)
	flat_atomic_add v[2:3], v235
	s_waitcnt vmcnt(0)

; __device__ __forceinline__ unsigned xb_ld(unsigned* p)              { return __hip_atomic_load(p, __ATOMIC_RELAXED, __HIP_MEMORY_SCOPE_AGENT); }
; __device__ __forceinline__ unsigned xb_add(unsigned* p, unsigned v) { return __hip_atomic_fetch_add(p, v, __ATOMIC_RELAXED, __HIP_MEMORY_SCOPE_AGENT); }
; #define XB_SPIN(cond, bar) do { unsigned _sp = 0; while (cond) { __builtin_amdgcn_s_sleep(1); \
;     if ((++_sp & 255u) == 0u) { if (xb_ld(&(bar)[XB_TMO])) break; if (_sp > XB_SPIN_CAP) { atomicAdd(&(bar)[XB_TMO], 1u); break; } } } } while (0)
; __device__ __forceinline__ void xcd_barrier(const XcdBarrier& b) {
;     ...
;         unsigned nloc = b.st[0], nx = b.st[1];
;         if (nloc == 0u) { xcd_barrier_complete(bar, b.x, nloc, nx); b.st[0] = nloc; b.st[1] = nx; }
;         const unsigned old = xb_add(&bar[XB_XSUB(b.x)], 1u);
;         const unsigned gen = old / nloc;
;         if (old + 1u == (gen + 1u) * nloc) {
;             __builtin_amdgcn_fence(__ATOMIC_RELEASE, "agent");
;             asm volatile("s_waitcnt vmcnt(0)" ::: "memory");
;             const unsigned og = xb_add(&bar[XB_TOP], 1u);
;             const unsigned tg = og / nx;
;             if (og + 1u == (tg + 1u) * nx) xb_add(&bar[XB_TOPGEN], 1u);
;             else XB_SPIN(xb_ld(&bar[XB_TOPGEN]) == tg, bar);
.LBB0_1272:
	s_lshl_b32 s2, s2, 6
	s_add_i32 s88, s2, 0x500
	s_lshl_b64 s[6:7], s[88:89], 2
	s_add_u32 s6, s46, s6
	s_addc_u32 s7, s47, s7
	v_mov_b64_e32 v[4:5], s[6:7]
	flat_atomic_add v4, v[4:5], v235 sc0
	buffer_inv sc1
	v_cvt_f32_u32_e32 v3, v2
	v_sub_u32_e32 v5, 0, v2
	v_rcp_iflag_f32_e32 v3, v3
	s_nop 0
	v_mul_f32_e32 v3, 0x4f7ffffe, v3
	v_cvt_u32_f32_e32 v3, v3
	v_mul_lo_u32 v5, v5, v3
	v_mul_hi_u32 v5, v3, v5
	v_add_u32_e32 v3, v3, v5
	s_waitcnt vmcnt(0) lgkmcnt(0)
	v_mul_hi_u32 v3, v4, v3
	v_mul_lo_u32 v5, v3, v2
	v_sub_u32_e32 v5, v4, v5
	v_cmp_ge_u32_e32 vcc, v5, v2
	v_add_u32_e32 v6, 1, v3
	s_nop 0
	v_cndmask_b32_e32 v3, v3, v6, vcc
	v_sub_u32_e32 v6, v5, v2
	v_cndmask_b32_e32 v5, v5, v6, vcc
	v_cmp_ge_u32_e32 vcc, v5, v2
	v_add_u32_e32 v5, 1, v3
	v_add_u32_e32 v6, 1, v4
	v_cndmask_b32_e32 v3, v3, v5, vcc
	v_mad_u64_u32 v[4:5], s[6:7], v2, v3, v[2:3]
	v_cmp_ne_u32_e32 vcc, v6, v4
	s_and_saveexec_b64 s[6:7], vcc
	s_xor_b64 s[10:11], exec, s[6:7]
	s_cbranch_execz .LBB0_1285
	s_add_i32 s88, s2, 0x900
	s_lshl_b64 s[6:7], s[88:89], 2
	s_add_u32 s14, s46, s6
	s_addc_u32 s15, s47, s7
	v_mov_b64_e32 v[4:5], s[14:15]
	flat_load_dword v0, v[4:5] sc1
	s_waitcnt vmcnt(0) lgkmcnt(0)
	v_cmp_eq_u32_e32 vcc, v0, v3
	s_and_saveexec_b64 s[12:13], vcc
	s_cbranch_execz .LBB0_1284
	s_mov_b32 s3, 1
	s_mov_b64 s[16:17], 0
	s_branch .LBB0_1276

; __device__ __forceinline__ unsigned xb_add(unsigned* p, unsigned v) { return __hip_atomic_fetch_add(p, v, __ATOMIC_RELAXED, __HIP_MEMORY_SCOPE_AGENT); }
; __device__ __forceinline__ void xcd_barrier(const XcdBarrier& b) {
;     ...
;             __builtin_amdgcn_fence(__ATOMIC_ACQUIRE, "agent");
;             xb_add(&bar[XB_XGEN(b.x)], 1u);
;             asm volatile("s_waitcnt vmcnt(0)" ::: "memory");
.LBB0_1300:
	s_or_b64 exec, exec, s[10:11]
	s_add_i32 s88, s2, 0x900
	s_lshl_b64 s[2:3], s[88:89], 2
	s_add_u32 s2, s46, s2
	s_addc_u32 s3, s47, s3
	v_mov_b64_e32 v[2:3], s[2:3]
	s_waitcnt vmcnt(0) lgkmcnt(0)
	flat_atomic_add v[2:3], v235
	s_waitcnt vmcnt(0)
